# mixer C: per-head sink logit load requested at the top of the query-head iteration instead of right before its use
# speedup vs baseline: 1.0139x; 1.0139x over previous
; #define LAS __attribute__((address_space(3)))
; __device__ __forceinline__ void mixer_c_shared(const bf16* CQ, const bf16* CK, const bf16* CV  , bf16* O, const float* rel_bias, const float* sink, LAS unsigned char* lds, int G, int blk, int tid, int lane, int wave) {
;     ...
;         for (int j = 0; j < 4; ++j) {
;             const int h = 4 * kvh + j; const LAS float* tab = tab4 + j * TC_LEN;
;             bf16x8 qf[4];
; #pragma unroll
;             for (int d0 = 0; d0 < 4; ++d0) qf[d0] = qn[d0];
;             if (j < 3) {
; #pragma unroll
;                 for (int d0 = 0; d0 < 4; ++d0) qn[d0] = *(const bf16x8*)(qp + 64 * (j + 1) + 16 * d0); }
;     ...
;               const float xs = fminf(fmaxf((sink[h] * LOG2E + 64.0f) * 128.0f, 0.0f), 32767.0f); const float ps = __uint_as_float(((unsigned)__float2int_rn(xs)) << 16);
.LBB0_1132:
	v_readlane_b32 s98, v254, 34
	v_readlane_b32 s99, v254, 35
	s_add_i32 s100, s25, s24
	s_lshl_b32 s100, s100, 2
	s_add_u32 s98, s98, s100
	s_addc_u32 s99, s99, 0
	global_load_dword v246, v3, s[98:99]
	s_cmp_eq_u32 s25, 3
	s_cbranch_scc1 .LBB0_1134
	s_lshl_b32 s16, s25, 7
	v_lshl_add_u64 v[4:5], v[144:145], 0, s[16:17]
	global_load_dwordx4 v[86:89], v[4:5], off offset:128
	global_load_dwordx4 v[90:93], v[4:5], off offset:160
	global_load_dwordx4 v[94:97], v[4:5], off offset:192
	global_load_dwordx4 v[98:101], v[4:5], off offset:224

; __device__ __forceinline__ void mixer_c_shared(const bf16* CQ, const bf16* CK, const bf16* CV  , bf16* O, const float* rel_bias, const float* sink, LAS unsigned char* lds, int G, int blk, int tid, int lane, int wave) {
;     ...
;               const float xs = fminf(fmaxf((sink[h] * LOG2E + 64.0f) * 128.0f, 0.0f), 32767.0f); const float ps = __uint_as_float(((unsigned)__float2int_rn(xs)) << 16);
;               const float la = __shfl(lsum[0], i5 & 15), lb = __shfl(lsum[1], i5 & 15); const float lt = ((i5 & 16) ? lb : la) + ps;
;               l = (hh == 0) ? lt : 0.0f;
;               const bool bad = ((orw & 0xC000C000u) != 0u) || !(lt > 1.0e-30f) || (sink[h] * LOG2E >= 63.0f);
;               if (__builtin_expect(__any(bad), 0)) {
.LBB0_1139:
	v_readlane_b32 s40, v254, 30
	s_add_i32 s16, s25, s24
	v_readlane_b32 s41, v254, 31
	v_readlane_b32 s44, v254, 34
	v_readlane_b32 s45, v254, 35
	s_lshl_b64 s[10:11], s[16:17], 2
	s_mov_b64 s[40:41], s[44:45]
	s_add_u32 s10, s40, s10
	s_addc_u32 s11, s41, s11
	s_nop 0
	ds_bpermute_b32 v4, v192, v4
	ds_bpermute_b32 v5, v192, v5
	v_and_b32_e32 v6, 0xc000c000, v8
	v_cmp_ne_u32_e32 vcc, 0, v6
	v_readlane_b32 s46, v254, 36
	v_readlane_b32 s47, v254, 37
	s_waitcnt lgkmcnt(0)
	v_cndmask_b32_e64 v4, v5, v4, s[4:5]
	v_readlane_b32 s48, v254, 38
	v_readlane_b32 s49, v254, 39
	v_readlane_b32 s50, v254, 40
	v_readlane_b32 s51, v254, 41
	v_readlane_b32 s52, v254, 42
	v_readlane_b32 s53, v254, 43
	v_readlane_b32 s54, v254, 44
	v_readlane_b32 s55, v254, 45
	s_mov_b64 s[44:45], s[48:49]
	v_readlane_b32 s42, v254, 32
	v_readlane_b32 s43, v254, 33
	s_mov_b64 s[46:47], s[50:51]
	s_mov_b64 s[48:49], s[52:53]
	s_mov_b64 s[50:51], s[54:55]
	s_waitcnt vmcnt(0)
	v_fmamk_f32 v203, v246, 0x3fb8aa3b, v142
	v_mul_f32_e32 v7, 0x43000000, v203
	v_max_f32_e32 v7, 0, v7
	v_min_f32_e32 v7, 0x46fffe00, v7
	v_rndne_f32_e32 v7, v7
	v_cvt_i32_f32_sdwa v7, v7 dst_sel:WORD_1 dst_unused:UNUSED_PAD src0_sel:DWORD
	v_mul_f32_e32 v5, 0x3fb8aa3b, v246
	v_add_f32_e32 v2, v4, v7
	v_cmp_nlt_f32_e64 s[10:11], s35, v2
	s_or_b64 s[10:11], vcc, s[10:11]
	v_cmp_le_f32_e32 vcc, s36, v5
	s_or_b64 vcc, s[10:11], vcc
	s_cbranch_vccnz .LBB0_1143
	v_cndmask_b32_e64 v202, 0, v2, s[6:7]
